# baseline (speedup 1.0000x reference)
.LBB0_16:
	s_mov_b32 exec_lo, 0
	v_mov_b32_e32 v225, 0
	v_mov_b32_e32 v226, 0
	s_mov_b32 exec_lo, -1
	s_waitcnt lgkmcnt(0)
	s_cmp_lg_u32 0, -1
	s_cselect_b32 s0, 0, 0
	s_addk_i32 s0, 0x4000
	s_mov_b32 s27, 0
	v_add_u32_e32 v215, s0, v184
	s_add_i32 s30, s28, 0x14c00
	s_mov_b32 s31, 0x41000000
.LBB0_17:
	v_mfma_f32_32x32x16_bf16 v[112:127], a[192:195], a[128:131], v[0:15]
	v_exp_f32_e32 v48, v48
	v_exp_f32_e32 v49, v49
	ds_read_b64_tr_b16 v[172:173], v215 offset:0
	v_cvt_pk_bf16_f32 v164, v128, v129
	v_exp_f32_e32 v50, v50
	v_exp_f32_e32 v51, v51
	v_mfma_f32_32x32x16_bf16 v[96:111], a[192:195], a[160:163], v[16:31]
	ds_read_b64_tr_b16 v[174:175], v215 offset:0x800
	v_cvt_pk_bf16_f32 v165, v130, v131
	v_mfma_f32_32x32x16_bf16 v[80:95], a[224:227], a[128:131], v[0:15]
	ds_read_b64_tr_b16 v[184:185], v215 offset:0x200
	v_exp_f32_e32 v239, v52
	v_exp_f32_e32 v240, v53
	v_cvt_pk_bf16_f32 v166, v132, v133
	v_mfma_f32_32x32x16_bf16 v[64:79], a[224:227], a[160:163], v[16:31]
	ds_read_b64_tr_b16 v[186:187], v215 offset:0xa00
	ds_read_b64_tr_b16 v[180:181], v215 offset:0x400
	v_exp_f32_e32 v241, v54
	v_exp_f32_e32 v242, v55
	v_cvt_pk_bf16_f32 v167, v134, v135
	v_exp_f32_e32 v227, v56
	v_exp_f32_e32 v228, v57
	v_mfma_f32_32x32x16_bf16 v[112:127], a[196:199], a[132:135], v[112:127]
	ds_read_b64_tr_b16 v[182:183], v215 offset:0xc00
	v_cvt_pk_bf16_f32 v128, v136, v137
	v_exp_f32_e32 v229, v58
	v_exp_f32_e32 v230, v59
	v_mfma_f32_32x32x16_bf16 v[96:111], a[196:199], a[164:167], v[96:111]
	ds_read_b64_tr_b16 v[188:189], v215 offset:0x600
	v_cvt_pk_bf16_f32 v129, v138, v139
	v_exp_f32_e32 v231, v60
	v_exp_f32_e32 v232, v61
	v_mfma_f32_32x32x16_bf16 v[80:95], a[228:231], a[132:135], v[80:95]
	ds_read_b64_tr_b16 v[190:191], v215 offset:0xe00
	v_cvt_pk_bf16_f32 v130, v140, v141
	v_mfma_f32_32x32x16_bf16 v[64:79], a[228:231], a[164:167], v[64:79]
	ds_read_b64_tr_b16 v[176:177], v215 offset:0x1000
	v_exp_f32_e32 v233, v62
	v_exp_f32_e32 v234, v63
	ds_read_b64_tr_b16 v[178:179], v215 offset:0x1800
	v_cvt_pk_bf16_f32 v131, v142, v143
	v_exp_f32_e32 v141, v32
	v_exp_f32_e32 v142, v33
	v_mfma_f32_32x32x16_bf16 v[112:127], a[200:203], a[136:139], v[112:127]
	ds_read_b64_tr_b16 v[168:169], v215 offset:0x1200
	v_cvt_pk_bf16_f32 v192, v144, v145
	v_exp_f32_e32 v143, v34
	v_mfma_f32_32x32x16_bf16 v[96:111], a[200:203], a[168:171], v[96:111]
	ds_read_b64_tr_b16 v[170:171], v215 offset:0x1a00
	v_exp_f32_e32 v243, v35
	v_cvt_pk_bf16_f32 v193, v146, v147
	v_mfma_f32_32x32x16_bf16 v[80:95], a[232:235], a[136:139], v[80:95]
	ds_read_b64_tr_b16 v[160:161], v215 offset:0x1400
	v_exp_f32_e32 v244, v36
	v_exp_f32_e32 v245, v37
	v_cvt_pk_bf16_f32 v194, v148, v149
	v_mfma_f32_32x32x16_bf16 v[64:79], a[232:235], a[168:171], v[64:79]
	ds_read_b64_tr_b16 v[162:163], v215 offset:0x1c00
	ds_read_b64_tr_b16 v[136:137], v215 offset:0x1600
	v_exp_f32_e32 v246, v38
	v_exp_f32_e32 v247, v39
	v_cvt_pk_bf16_f32 v195, v150, v151
	v_exp_f32_e32 v148, v40
	v_exp_f32_e32 v149, v41
	v_mfma_f32_32x32x16_bf16 v[112:127], a[204:207], a[140:143], v[112:127]
	ds_read_b64_tr_b16 v[138:139], v215 offset:0x1e00
	v_cvt_pk_bf16_f32 v144, v152, v153
	v_exp_f32_e32 v150, v42
	v_exp_f32_e32 v151, v43
	v_mfma_f32_32x32x16_bf16 v[96:111], a[204:207], a[172:175], v[96:111]
	ds_read_b64_tr_b16 v[132:133], v215 offset:0x2000
	v_cvt_pk_bf16_f32 v145, v154, v155
	v_exp_f32_e32 v152, v44
	v_exp_f32_e32 v153, v45
	v_mfma_f32_32x32x16_bf16 v[80:95], a[236:239], a[140:143], v[80:95]
	ds_read_b64_tr_b16 v[134:135], v215 offset:0x2800
	v_cvt_pk_bf16_f32 v146, v156, v157
	v_mfma_f32_32x32x16_bf16 v[64:79], a[236:239], a[172:175], v[64:79]
	ds_read_b64_tr_b16 v[60:61], v215 offset:0x2200
	v_exp_f32_e32 v154, v46
	v_exp_f32_e32 v155, v47
	ds_read_b64_tr_b16 v[62:63], v215 offset:0x2a00
	v_cvt_pk_bf16_f32 v147, v158, v159
	s_mov_b32 s0, s29
	v_mfma_f32_32x32x16_bf16 v[112:127], a[208:211], a[144:147], v[112:127]
	ds_read_b64_tr_b16 v[56:57], v215 offset:0x2400
	v_cvt_pk_bf16_f32 v52, v48, v49
	v_add_f32_e32 v32, v236, v48
	v_add_f32_e32 v33, v235, v49
	s_add_i32 s57, s58, s59
	s_and_b32 s57, s57, 0x7ffff
	s_mov_b32 s33, s57
	s_mov_b32 s1, s33
	v_mfma_f32_32x32x16_bf16 v[96:111], a[208:211], a[176:179], v[96:111]
	ds_read_b64_tr_b16 v[58:59], v215 offset:0x2c00
	v_cvt_pk_bf16_f32 v53, v50, v51
	v_add_f32_e32 v32, v32, v50
	v_add_f32_e32 v33, v33, v51
	s_mov_b32 s35, s20
	v_mfma_f32_32x32x16_bf16 v[80:95], a[240:243], a[144:147], v[80:95]
	ds_read_b64_tr_b16 v[48:49], v215 offset:0x2600
	v_cvt_pk_bf16_f32 v54, v239, v240
	v_add_f32_e32 v32, v32, v239
	v_add_f32_e32 v33, v33, v240
	s_add_i32 s36, s57, 0x400
	v_mfma_f32_32x32x16_bf16 v[64:79], a[240:243], a[176:179], v[64:79]
	ds_read_b64_tr_b16 v[50:51], v215 offset:0x2e00
	ds_read_b64_tr_b16 v[44:45], v215 offset:0x3000
	v_cvt_pk_bf16_f32 v55, v241, v242
	v_add_f32_e32 v32, v32, v241
	v_add_f32_e32 v33, v33, v242
	s_mov_b32 s37, s21
	v_mfma_f32_32x32x16_bf16 v[112:127], a[212:215], a[148:151], v[112:127]
	ds_read_b64_tr_b16 v[46:47], v215 offset:0x3800
	v_add_f32_e32 v32, v32, v227
	v_add_f32_e32 v33, v33, v228
	s_add_i32 s34, s57, 0x800
	s_mov_b32 s38, s34
	v_mfma_f32_32x32x16_bf16 v[96:111], a[212:215], a[180:183], v[96:111]
	ds_read_b64_tr_b16 v[40:41], v215 offset:0x3200
	v_add_f32_e32 v32, v32, v229
	v_add_f32_e32 v33, v33, v230
	s_mov_b32 s39, s22
	v_mfma_f32_32x32x16_bf16 v[80:95], a[244:247], a[148:151], v[80:95]
	ds_read_b64_tr_b16 v[42:43], v215 offset:0x3a00
	v_add_f32_e32 v32, v32, v231
	v_add_f32_e32 v33, v33, v232
	s_add_i32 s40, s57, 0xc00
	v_mfma_f32_32x32x16_bf16 v[64:79], a[244:247], a[180:183], v[64:79]
	ds_read_b64_tr_b16 v[36:37], v215 offset:0x3400
	ds_read_b64_tr_b16 v[38:39], v215 offset:0x3c00
	v_add_f32_e32 v156, v32, v233
	v_add_f32_e32 v157, v33, v234
	s_mov_b32 s41, s23
	v_mfma_f32_32x32x16_bf16 v[112:127], a[216:219], a[152:155], v[112:127]
	ds_read_b64_tr_b16 v[32:33], v215 offset:0x3600
	v_cvt_pk_bf16_f32 v140, v141, v142
	v_add_f32_e32 v158, v237, v141
	v_add_f32_e32 v142, v238, v142
	s_mov_b32 s42, s58
	v_mfma_f32_32x32x16_bf16 v[96:111], a[216:219], a[184:187], v[96:111]
	ds_read_b64_tr_b16 v[34:35], v215 offset:0x3e00
	v_cvt_pk_bf16_f32 v141, v143, v243
	v_add_f32_e32 v143, v158, v143
	v_add_f32_e32 v158, v142, v243
	v_mfma_f32_32x32x16_bf16 v[80:95], a[248:251], a[152:155], v[80:95]
	s_mov_b32 s43, s24
	v_cvt_pk_bf16_f32 v142, v244, v245
	v_add_f32_e32 v159, v143, v244
	v_add_f32_e32 v158, v158, v245
	v_mfma_f32_32x32x16_bf16 v[64:79], a[248:251], a[184:187], v[64:79]
	s_add_i32 s44, s58, 0x80
	v_cvt_pk_bf16_f32 v143, v246, v247
	v_add_f32_e32 v159, v159, v246
	v_add_f32_e32 v158, v158, v247
	v_mfma_f32_32x32x16_bf16 v[112:127], a[220:223], a[156:159], v[112:127]
	s_mov_b32 s45, s25
	v_add_f32_e32 v159, v159, v148
	v_add_f32_e32 v158, v158, v149
	v_mfma_f32_32x32x16_bf16 v[96:111], a[220:223], a[188:191], v[96:111]
	s_add_i32 s46, s58, 0x800
	v_add_f32_e32 v159, v159, v150
	v_add_f32_e32 v158, v158, v151
	v_mfma_f32_32x32x16_bf16 v[80:95], a[252:255], a[156:159], v[80:95]
	s_mov_b32 s47, s26
	v_add_f32_e32 v159, v159, v152
	v_add_f32_e32 v158, v158, v153
	v_mfma_f32_32x32x16_bf16 v[64:79], a[252:255], a[188:191], v[64:79]
	s_add_i32 s48, s58, 0x880
	v_add_f32_e32 v159, v159, v154
	v_add_f32_e32 v158, v158, v155
	v_add_f32_e32 v156, v156, v157
	s_waitcnt vmcnt(0) lgkmcnt(0)
	s_barrier
	s_mov_b32 m0, s0
	v_mfma_f32_32x32x16_bf16 a[0:15], v[172:175], v[164:167], a[0:15]
	buffer_load_dwordx4 v222, s[12:15], s1 offen lds
	s_mov_b32 m0, s35
	v_mfma_f32_32x32x16_bf16 a[16:31], v[172:175], v[192:195], a[16:31]
	buffer_load_dwordx4 v223, s[12:15], s36 offen lds
	ds_read_b128 a[192:195], v217 offset:0
	s_mov_b32 m0, s37
	v_mfma_f32_32x32x16_bf16 a[32:47], v[184:187], v[164:167], a[32:47]
	v_add_f32_e32 v225, v225, v156
	v_add_f32_e32 v156, v159, v158
	buffer_load_dwordx4 v222, s[12:15], s38 offen lds
	ds_read_b128 a[196:199], v199 offset:0
	s_mov_b32 m0, s39
	v_mfma_f32_32x32x16_bf16 a[48:63], v[184:187], v[192:195], a[48:63]
	buffer_load_dwordx4 v223, s[12:15], s40 offen lds
	ds_read_b128 a[200:203], v198 offset:0
	s_mov_b32 m0, s41
	v_mfma_f32_32x32x16_bf16 a[64:79], v[180:183], v[164:167], a[64:79]
	v_add_f32_e32 v226, v226, v156
	buffer_load_dwordx4 v196, s[4:7], s42 offen lds
	ds_read_b128 a[204:207], v197 offset:0
	s_mov_b32 m0, s43
	v_mfma_f32_32x32x16_bf16 a[80:95], v[180:183], v[192:195], a[80:95]
	buffer_load_dwordx4 v196, s[4:7], s44 offen lds
	ds_read_b128 a[208:211], v217 offset:128
	s_mov_b32 m0, s45
	v_mfma_f32_32x32x16_bf16 a[96:111], v[188:191], v[164:167], a[96:111]
	buffer_load_dwordx4 v196, s[4:7], s46 offen lds
	ds_read_b128 a[212:215], v199 offset:128
	s_mov_b32 m0, s47
	v_mfma_f32_32x32x16_bf16 a[112:127], v[188:191], v[192:195], a[112:127]
	buffer_load_dwordx4 v196, s[4:7], s48 offen lds
	ds_read_b128 a[216:219], v198 offset:128
	s_nop 0
	v_mfma_f32_32x32x16_bf16 a[0:15], v[176:179], v[128:131], a[0:15]
	ds_read_b128 a[220:223], v197 offset:128
	s_cmp_gt_u32 s27, 12
	s_cbranch_scc1 .Lka_done
	s_cmp_gt_u32 s27, 4
	s_cbranch_scc1 .Lka_single
	v_cvt_pk_bf16_f32 v248, v248, v249
	v_cvt_pk_bf16_f32 v249, v250, v251
	v_cvt_pk_bf16_f32 v250, v252, v253
	v_cvt_pk_bf16_f32 v251, v254, v255
	v_lshrrev_b32_e32 v252, 1, v208
	buffer_store_dwordx4 v[248:251], v252, s[12:15], s56 offen sc1
	v_mbcnt_lo_u32_b32 v253, -1, 0
	v_mbcnt_hi_u32_b32 v253, -1, v253
	v_lshlrev_b32_e32 v253, 4, v253
	v_add_u32_e32 v253, s84, v253
	ds_read_b128 v[248:251], v253
	ds_read_b128 v[252:255], v253 offset:1024
	s_cmp_eq_u32 s27, 2
	s_cbranch_scc0 .Lka_nopub
	s_cmp_eq_u32 s50, 0
	s_cbranch_scc0 .Lf1_pub_done
	v_mov_b32_e32 v210, s70
	s_mov_b64 exec, 1
	global_store_dword v209, v210, s[72:73] offset:3072 sc1
	s_mov_b64 exec, -1

.LBB0_19:
	s_waitcnt lgkmcnt(0)
	v_mfma_f32_32x32x16_bf16 v[112:127], a[192:195], a[128:131], v[0:15]
	v_exp_f32_e32 v80, v80
	v_exp_f32_e32 v81, v81
	ds_read_b64_tr_b16 v[180:181], v212 offset:0
	v_cvt_pk_bf16_f32 v168, v128, v129
	v_exp_f32_e32 v82, v82
	v_exp_f32_e32 v83, v83
	v_mfma_f32_32x32x16_bf16 v[96:111], a[192:195], a[160:163], v[16:31]
	ds_read_b64_tr_b16 v[182:183], v212 offset:0x800
	v_cvt_pk_bf16_f32 v169, v130, v131
	v_mfma_f32_32x32x16_bf16 v[48:63], a[224:227], a[128:131], v[0:15]
	ds_read_b64_tr_b16 v[184:185], v212 offset:0x200
	v_exp_f32_e32 v239, v84
	v_exp_f32_e32 v240, v85
	v_cvt_pk_bf16_f32 v170, v132, v133
	v_mfma_f32_32x32x16_bf16 v[32:47], a[224:227], a[160:163], v[16:31]
	ds_read_b64_tr_b16 v[186:187], v212 offset:0xa00
	ds_read_b64_tr_b16 v[176:177], v212 offset:0x400
	v_exp_f32_e32 v241, v86
	v_exp_f32_e32 v242, v87
	v_cvt_pk_bf16_f32 v171, v134, v135
	v_exp_f32_e32 v227, v88
	v_exp_f32_e32 v228, v89
	v_mfma_f32_32x32x16_bf16 v[112:127], a[196:199], a[132:135], v[112:127]
	ds_read_b64_tr_b16 v[178:179], v212 offset:0xc00
	v_cvt_pk_bf16_f32 v128, v136, v137
	v_exp_f32_e32 v229, v90
	v_exp_f32_e32 v230, v91
	v_mfma_f32_32x32x16_bf16 v[96:111], a[196:199], a[164:167], v[96:111]
	ds_read_b64_tr_b16 v[188:189], v212 offset:0x600
	v_cvt_pk_bf16_f32 v129, v138, v139
	v_exp_f32_e32 v231, v92
	v_exp_f32_e32 v232, v93
	v_mfma_f32_32x32x16_bf16 v[48:63], a[228:231], a[132:135], v[48:63]
	ds_read_b64_tr_b16 v[190:191], v212 offset:0xe00
	v_cvt_pk_bf16_f32 v130, v140, v141
	v_mfma_f32_32x32x16_bf16 v[32:47], a[228:231], a[164:167], v[32:47]
	ds_read_b64_tr_b16 v[172:173], v212 offset:0x1000
	v_exp_f32_e32 v233, v94
	v_exp_f32_e32 v234, v95
	ds_read_b64_tr_b16 v[174:175], v212 offset:0x1800
	v_cvt_pk_bf16_f32 v131, v142, v143
	v_exp_f32_e32 v141, v64
	v_exp_f32_e32 v142, v65
	v_mfma_f32_32x32x16_bf16 v[112:127], a[200:203], a[136:139], v[112:127]
	ds_read_b64_tr_b16 v[164:165], v212 offset:0x1200
	v_cvt_pk_bf16_f32 v192, v144, v145
	v_exp_f32_e32 v143, v66
	v_mfma_f32_32x32x16_bf16 v[96:111], a[200:203], a[168:171], v[96:111]
	ds_read_b64_tr_b16 v[166:167], v212 offset:0x1a00
	v_exp_f32_e32 v243, v67
	v_cvt_pk_bf16_f32 v193, v146, v147
	v_mfma_f32_32x32x16_bf16 v[48:63], a[232:235], a[136:139], v[48:63]
	ds_read_b64_tr_b16 v[160:161], v212 offset:0x1400
	v_exp_f32_e32 v244, v68
	v_exp_f32_e32 v245, v69
	v_cvt_pk_bf16_f32 v194, v148, v149
	v_mfma_f32_32x32x16_bf16 v[32:47], a[232:235], a[168:171], v[32:47]
	ds_read_b64_tr_b16 v[162:163], v212 offset:0x1c00
	ds_read_b64_tr_b16 v[136:137], v212 offset:0x1600
	v_exp_f32_e32 v246, v70
	v_exp_f32_e32 v247, v71
	v_cvt_pk_bf16_f32 v195, v150, v151
	v_exp_f32_e32 v148, v72
	v_exp_f32_e32 v149, v73
	v_mfma_f32_32x32x16_bf16 v[112:127], a[204:207], a[140:143], v[112:127]
	ds_read_b64_tr_b16 v[138:139], v212 offset:0x1e00
	v_cvt_pk_bf16_f32 v144, v152, v153
	v_exp_f32_e32 v150, v74
	v_exp_f32_e32 v151, v75
	v_mfma_f32_32x32x16_bf16 v[96:111], a[204:207], a[172:175], v[96:111]
	ds_read_b64_tr_b16 v[132:133], v212 offset:0x2000
	v_cvt_pk_bf16_f32 v145, v154, v155
	v_exp_f32_e32 v152, v76
	v_exp_f32_e32 v153, v77
	v_mfma_f32_32x32x16_bf16 v[48:63], a[236:239], a[140:143], v[48:63]
	ds_read_b64_tr_b16 v[134:135], v212 offset:0x2800
	v_cvt_pk_bf16_f32 v146, v156, v157
	v_mfma_f32_32x32x16_bf16 v[32:47], a[236:239], a[172:175], v[32:47]
	ds_read_b64_tr_b16 v[92:93], v212 offset:0x2200
	v_exp_f32_e32 v154, v78
	v_exp_f32_e32 v155, v79
	ds_read_b64_tr_b16 v[94:95], v212 offset:0x2a00
	v_cvt_pk_bf16_f32 v147, v158, v159
	s_mov_b32 s0, s3
	v_mfma_f32_32x32x16_bf16 v[112:127], a[208:211], a[144:147], v[112:127]
	ds_read_b64_tr_b16 v[88:89], v212 offset:0x2400
	v_cvt_pk_bf16_f32 v84, v80, v81
	v_add_f32_e32 v64, v236, v80
	v_add_f32_e32 v65, v235, v81
	s_add_i32 s58, s57, s60
	s_and_b32 s58, s58, 0x7ffff
	s_mov_b32 s1, s58
	v_mfma_f32_32x32x16_bf16 v[96:111], a[208:211], a[176:179], v[96:111]
	ds_read_b64_tr_b16 v[90:91], v212 offset:0x2c00
	v_cvt_pk_bf16_f32 v85, v82, v83
	v_add_f32_e32 v64, v64, v82
	v_add_f32_e32 v65, v65, v83
	s_mov_b32 s35, s10
	v_mfma_f32_32x32x16_bf16 v[48:63], a[240:243], a[144:147], v[48:63]
	ds_read_b64_tr_b16 v[80:81], v212 offset:0x2600
	v_cvt_pk_bf16_f32 v86, v239, v240
	v_add_f32_e32 v64, v64, v239
	v_add_f32_e32 v65, v65, v240
	s_add_i32 s36, s58, 0x400
	v_mfma_f32_32x32x16_bf16 v[32:47], a[240:243], a[176:179], v[32:47]
	ds_read_b64_tr_b16 v[82:83], v212 offset:0x2e00
	ds_read_b64_tr_b16 v[76:77], v212 offset:0x3000
	v_cvt_pk_bf16_f32 v87, v241, v242
	v_add_f32_e32 v64, v64, v241
	v_add_f32_e32 v65, v65, v242
	s_mov_b32 s37, s11
	v_mfma_f32_32x32x16_bf16 v[112:127], a[212:215], a[148:151], v[112:127]
	ds_read_b64_tr_b16 v[78:79], v212 offset:0x3800
	v_add_f32_e32 v64, v64, v227
	v_add_f32_e32 v65, v65, v228
	s_add_i32 s38, s58, 0x800
	v_mfma_f32_32x32x16_bf16 v[96:111], a[212:215], a[180:183], v[96:111]
	ds_read_b64_tr_b16 v[72:73], v212 offset:0x3200
	v_add_f32_e32 v64, v64, v229
	v_add_f32_e32 v65, v65, v230
	s_mov_b32 s39, s16
	v_mfma_f32_32x32x16_bf16 v[48:63], a[244:247], a[148:151], v[48:63]
	ds_read_b64_tr_b16 v[74:75], v212 offset:0x3a00
	v_add_f32_e32 v64, v64, v231
	v_add_f32_e32 v65, v65, v232
	s_add_i32 s40, s58, 0xc00
	v_mfma_f32_32x32x16_bf16 v[32:47], a[244:247], a[180:183], v[32:47]
	ds_read_b64_tr_b16 v[68:69], v212 offset:0x3400
	ds_read_b64_tr_b16 v[70:71], v212 offset:0x3c00
	v_add_f32_e32 v156, v64, v233
	v_add_f32_e32 v157, v65, v234
	s_mov_b32 s41, s2
	v_mfma_f32_32x32x16_bf16 v[112:127], a[216:219], a[152:155], v[112:127]
	ds_read_b64_tr_b16 v[64:65], v212 offset:0x3600
	v_cvt_pk_bf16_f32 v140, v141, v142
	v_add_f32_e32 v158, v237, v141
	v_add_f32_e32 v142, v238, v142
	v_mfma_f32_32x32x16_bf16 v[96:111], a[216:219], a[184:187], v[96:111]
	ds_read_b64_tr_b16 v[66:67], v212 offset:0x3e00
	v_cvt_pk_bf16_f32 v141, v143, v243
	v_add_f32_e32 v143, v158, v143
	v_add_f32_e32 v158, v142, v243
	v_mfma_f32_32x32x16_bf16 v[48:63], a[248:251], a[152:155], v[48:63]
	s_mov_b32 s42, s17
	v_cvt_pk_bf16_f32 v142, v244, v245
	v_add_f32_e32 v159, v143, v244
	v_add_f32_e32 v158, v158, v245
	v_mfma_f32_32x32x16_bf16 v[32:47], a[248:251], a[184:187], v[32:47]
	s_add_i32 s43, s57, 0x80
	v_cvt_pk_bf16_f32 v143, v246, v247
	v_add_f32_e32 v159, v159, v246
	v_add_f32_e32 v158, v158, v247
	v_mfma_f32_32x32x16_bf16 v[112:127], a[220:223], a[156:159], v[112:127]
	s_mov_b32 s44, s18
	v_add_f32_e32 v159, v159, v148
	v_add_f32_e32 v158, v158, v149
	v_mfma_f32_32x32x16_bf16 v[96:111], a[220:223], a[188:191], v[96:111]
	v_add_f32_e32 v159, v159, v150
	v_add_f32_e32 v158, v158, v151
	v_mfma_f32_32x32x16_bf16 v[48:63], a[252:255], a[156:159], v[48:63]
	s_mov_b32 s45, s19
	v_add_f32_e32 v159, v159, v152
	v_add_f32_e32 v158, v158, v153
	v_mfma_f32_32x32x16_bf16 v[32:47], a[252:255], a[188:191], v[32:47]
	s_add_i32 s46, s57, 0x880
	v_add_f32_e32 v159, v159, v154
	v_add_f32_e32 v158, v158, v155
	v_add_f32_e32 v156, v156, v157
	s_waitcnt vmcnt(0) lgkmcnt(0)
	s_barrier
	s_mov_b32 m0, s0
	v_mfma_f32_32x32x16_bf16 a[0:15], v[180:183], v[168:171], a[0:15]
	buffer_load_dwordx4 v222, s[12:15], s1 offen lds
	s_mov_b32 m0, s35
	v_mfma_f32_32x32x16_bf16 a[16:31], v[180:183], v[192:195], a[16:31]
	buffer_load_dwordx4 v223, s[12:15], s36 offen lds
	ds_read_b128 a[192:195], v218 offset:0
	s_mov_b32 m0, s37
	v_mfma_f32_32x32x16_bf16 a[32:47], v[184:187], v[168:171], a[32:47]
	v_add_f32_e32 v225, v225, v156
	v_add_f32_e32 v156, v159, v158
	buffer_load_dwordx4 v222, s[12:15], s38 offen lds
	ds_read_b128 a[196:199], v219 offset:0
	s_mov_b32 m0, s39
	v_mfma_f32_32x32x16_bf16 a[48:63], v[184:187], v[192:195], a[48:63]
	buffer_load_dwordx4 v223, s[12:15], s40 offen lds
	ds_read_b128 a[200:203], v220 offset:0
	s_mov_b32 m0, s41
	v_mfma_f32_32x32x16_bf16 a[64:79], v[176:179], v[168:171], a[64:79]
	v_add_f32_e32 v226, v226, v156
	buffer_load_dwordx4 v196, s[4:7], s33 offen lds
	ds_read_b128 a[204:207], v221 offset:0
	s_mov_b32 m0, s42
	v_mfma_f32_32x32x16_bf16 a[80:95], v[176:179], v[192:195], a[80:95]
	buffer_load_dwordx4 v196, s[4:7], s43 offen lds
	ds_read_b128 a[208:211], v218 offset:128
	s_mov_b32 m0, s44
	v_mfma_f32_32x32x16_bf16 a[96:111], v[188:191], v[168:171], a[96:111]
	buffer_load_dwordx4 v196, s[4:7], s34 offen lds
	ds_read_b128 a[212:215], v219 offset:128
	s_mov_b32 m0, s45
	v_mfma_f32_32x32x16_bf16 a[112:127], v[188:191], v[192:195], a[112:127]
	buffer_load_dwordx4 v196, s[4:7], s46 offen lds
	ds_read_b128 a[216:219], v220 offset:128
	s_nop 0
	v_mfma_f32_32x32x16_bf16 a[0:15], v[172:175], v[128:131], a[0:15]
	ds_read_b128 a[220:223], v221 offset:128
	s_cmp_gt_u32 s27, 12
	s_cbranch_scc1 .Lkc_done
	s_cmp_gt_u32 s27, 4
	s_cbranch_scc1 .Lkc_single
	v_cvt_pk_bf16_f32 v248, v248, v249
	v_cvt_pk_bf16_f32 v249, v250, v251
	v_cvt_pk_bf16_f32 v250, v252, v253
	v_cvt_pk_bf16_f32 v251, v254, v255
	v_lshrrev_b32_e32 v252, 1, v208
	buffer_store_dwordx4 v[248:251], v252, s[12:15], s56 offen sc1
	v_mbcnt_lo_u32_b32 v253, -1, 0
	v_mbcnt_hi_u32_b32 v253, -1, v253
	v_lshlrev_b32_e32 v253, 4, v253
	v_add_u32_e32 v253, s84, v253
	ds_read_b128 v[248:251], v253
	ds_read_b128 v[252:255], v253 offset:1024
	s_branch .Lkc_done

.LBB0_36:
	v_mov_b32_e32 v200, v225
	v_mov_b32_e32 v201, v226
	s_nop 1
	v_permlane32_swap_b32_e32 v225, v200
	v_permlane32_swap_b32_e32 v226, v201
	v_add_f32_e32 v225, v225, v200
	v_add_f32_e32 v226, v226, v201
	s_lshl_b32 s53, s50, 6
	s_add_i32 s53, s53, s52
	v_mov_b32_e32 v200, s53
	s_lshl_b32 s53, s50, 14
	s_add_i32 s53, s53, 0x10000
	v_mov_b32_e32 v201, s53
	v_mbcnt_lo_u32_b32 v204, -1, 0
	v_mbcnt_hi_u32_b32 v204, -1, v204
	v_lshrrev_b32_e32 v202, 4, v204
	v_add_u32_e32 v203, 4, v202
	v_add_u32_e32 v205, 8, v202
	v_add_u32_e32 v206, 12, v202
	v_add_u32_e32 v207, 16, v202
	v_add_u32_e32 v208, 20, v202
	v_add_u32_e32 v209, 24, v202
	v_add_u32_e32 v210, 28, v202
	v_mfma_f32_32x32x16_bf16 v[112:127], a[192:195], a[128:131], v[0:15]
	v_exp_f32_e32 v48, v48
	v_exp_f32_e32 v49, v49
	ds_read_b64_tr_b16 v[180:181], v215 offset:0
	v_cvt_pk_bf16_f32 v164, v128, v129
	v_exp_f32_e32 v50, v50
	v_exp_f32_e32 v51, v51
	v_mfma_f32_32x32x16_bf16 v[96:111], a[192:195], a[160:163], v[16:31]
	ds_read_b64_tr_b16 v[182:183], v215 offset:0x800
	v_cvt_pk_bf16_f32 v165, v130, v131
	v_mfma_f32_32x32x16_bf16 v[80:95], a[224:227], a[128:131], v[0:15]
	v_exp_f32_e32 v218, v52
	v_exp_f32_e32 v219, v53
	ds_read_b64_tr_b16 v[188:189], v215 offset:0x200
	v_cvt_pk_bf16_f32 v166, v132, v133
	v_mfma_f32_32x32x16_bf16 v[64:79], a[224:227], a[160:163], v[16:31]
	ds_read_b64_tr_b16 v[190:191], v215 offset:0xa00
	ds_read_b64_tr_b16 v[176:177], v215 offset:0x400
	v_exp_f32_e32 v230, v54
	v_exp_f32_e32 v231, v55
	v_cvt_pk_bf16_f32 v167, v134, v135
	v_exp_f32_e32 v220, v56
	v_exp_f32_e32 v221, v57
	v_mfma_f32_32x32x16_bf16 v[112:127], a[196:199], a[132:135], v[112:127]
	ds_read_b64_tr_b16 v[178:179], v215 offset:0xc00
	v_cvt_pk_bf16_f32 v128, v136, v137
	v_exp_f32_e32 v222, v58
	v_exp_f32_e32 v223, v59
	v_mfma_f32_32x32x16_bf16 v[96:111], a[196:199], a[164:167], v[96:111]
	ds_read_b64_tr_b16 v[184:185], v215 offset:0x600
	v_cvt_pk_bf16_f32 v129, v138, v139
	v_exp_f32_e32 v224, v60
	v_exp_f32_e32 v227, v61
	v_mfma_f32_32x32x16_bf16 v[80:95], a[228:231], a[132:135], v[80:95]
	ds_read_b64_tr_b16 v[186:187], v215 offset:0xe00
	v_cvt_pk_bf16_f32 v130, v140, v141
	v_mfma_f32_32x32x16_bf16 v[64:79], a[228:231], a[164:167], v[64:79]
	ds_read_b64_tr_b16 v[172:173], v215 offset:0x1000
	v_exp_f32_e32 v228, v62
	v_exp_f32_e32 v229, v63
	ds_read_b64_tr_b16 v[174:175], v215 offset:0x1800
	v_cvt_pk_bf16_f32 v131, v142, v143
	v_exp_f32_e32 v141, v32
	v_exp_f32_e32 v142, v33
	v_mfma_f32_32x32x16_bf16 v[112:127], a[200:203], a[136:139], v[112:127]
	ds_read_b64_tr_b16 v[168:169], v215 offset:0x1200
	v_cvt_pk_bf16_f32 v192, v144, v145
	v_exp_f32_e32 v143, v34
	v_mfma_f32_32x32x16_bf16 v[96:111], a[200:203], a[168:171], v[96:111]
	ds_read_b64_tr_b16 v[170:171], v215 offset:0x1a00
	v_exp_f32_e32 v232, v35
	v_cvt_pk_bf16_f32 v193, v146, v147
	v_mfma_f32_32x32x16_bf16 v[80:95], a[232:235], a[136:139], v[80:95]
	ds_read_b64_tr_b16 v[160:161], v215 offset:0x1400
	v_exp_f32_e32 v233, v36
	v_exp_f32_e32 v234, v37
	v_cvt_pk_bf16_f32 v194, v148, v149
	v_mfma_f32_32x32x16_bf16 v[64:79], a[232:235], a[168:171], v[64:79]
	ds_read_b64_tr_b16 v[162:163], v215 offset:0x1c00
	ds_read_b64_tr_b16 v[136:137], v215 offset:0x1600
	v_exp_f32_e32 v239, v38
	v_exp_f32_e32 v240, v39
	v_cvt_pk_bf16_f32 v195, v150, v151
	v_exp_f32_e32 v148, v40
	v_exp_f32_e32 v149, v41
	v_mfma_f32_32x32x16_bf16 v[112:127], a[204:207], a[140:143], v[112:127]
	ds_read_b64_tr_b16 v[138:139], v215 offset:0x1e00
	v_cvt_pk_bf16_f32 v144, v152, v153
	v_exp_f32_e32 v150, v42
	v_exp_f32_e32 v151, v43
	v_mfma_f32_32x32x16_bf16 v[96:111], a[204:207], a[172:175], v[96:111]
	ds_read_b64_tr_b16 v[132:133], v215 offset:0x2000
	v_cvt_pk_bf16_f32 v145, v154, v155
	v_exp_f32_e32 v152, v44
	v_exp_f32_e32 v153, v45
	v_mfma_f32_32x32x16_bf16 v[80:95], a[236:239], a[140:143], v[80:95]
	ds_read_b64_tr_b16 v[134:135], v215 offset:0x2800
	v_cvt_pk_bf16_f32 v146, v156, v157
	v_mfma_f32_32x32x16_bf16 v[64:79], a[236:239], a[172:175], v[64:79]
	ds_read_b64_tr_b16 v[60:61], v215 offset:0x2200
	v_exp_f32_e32 v154, v46
	v_exp_f32_e32 v155, v47
	ds_read_b64_tr_b16 v[62:63], v215 offset:0x2a00
	v_cvt_pk_bf16_f32 v147, v158, v159
	v_mfma_f32_32x32x16_bf16 v[112:127], a[208:211], a[144:147], v[112:127]
	ds_read_b64_tr_b16 v[56:57], v215 offset:0x2400
	v_cvt_pk_bf16_f32 v52, v48, v49
	v_add_f32_e32 v32, v236, v48
	v_add_f32_e32 v33, v235, v49
	s_add_i32 s12, s28, 0x80000
	s_mov_b32 s0, s12
	v_mfma_f32_32x32x16_bf16 v[96:111], a[208:211], a[176:179], v[96:111]
	ds_read_b64_tr_b16 v[58:59], v215 offset:0x2c00
	v_cvt_pk_bf16_f32 v53, v50, v51
	v_add_f32_e32 v32, v32, v50
	v_add_f32_e32 v33, v33, v51
	v_mfma_f32_32x32x16_bf16 v[80:95], a[240:243], a[144:147], v[80:95]
	ds_read_b64_tr_b16 v[48:49], v215 offset:0x2600
	v_cvt_pk_bf16_f32 v54, v218, v219
	v_add_f32_e32 v32, v32, v218
	v_add_f32_e32 v33, v33, v219
	s_add_i32 s1, s28, 0x80400
	v_mfma_f32_32x32x16_bf16 v[64:79], a[240:243], a[176:179], v[64:79]
	ds_read_b64_tr_b16 v[50:51], v215 offset:0x2e00
	ds_read_b64_tr_b16 v[44:45], v215 offset:0x3000
	v_cvt_pk_bf16_f32 v55, v230, v231
	v_add_f32_e32 v32, v32, v230
	v_add_f32_e32 v33, v33, v231
	v_mfma_f32_32x32x16_bf16 v[112:127], a[212:215], a[148:151], v[112:127]
	ds_read_b64_tr_b16 v[46:47], v215 offset:0x3800
	v_add_f32_e32 v32, v32, v220
	v_add_f32_e32 v33, v33, v221
	s_add_i32 s13, s28, 0x80800
	s_mov_b32 s14, s13
	v_mfma_f32_32x32x16_bf16 v[96:111], a[212:215], a[180:183], v[96:111]
	ds_read_b64_tr_b16 v[40:41], v215 offset:0x3200
	v_add_f32_e32 v32, v32, v222
	v_add_f32_e32 v33, v33, v223
	v_mfma_f32_32x32x16_bf16 v[80:95], a[244:247], a[148:151], v[80:95]
	ds_read_b64_tr_b16 v[42:43], v215 offset:0x3a00
	v_add_f32_e32 v32, v32, v224
	v_add_f32_e32 v33, v33, v227
	s_add_i32 s15, s28, 0x80c00
	v_mfma_f32_32x32x16_bf16 v[64:79], a[244:247], a[180:183], v[64:79]
	ds_read_b64_tr_b16 v[36:37], v215 offset:0x3400
	ds_read_b64_tr_b16 v[38:39], v215 offset:0x3c00
	v_add_f32_e32 v156, v32, v228
	v_add_f32_e32 v157, v33, v229
	v_mfma_f32_32x32x16_bf16 v[112:127], a[216:219], a[152:155], v[112:127]
	ds_read_b64_tr_b16 v[32:33], v215 offset:0x3600
	v_cvt_pk_bf16_f32 v140, v141, v142
	v_add_f32_e32 v158, v237, v141
	v_add_f32_e32 v142, v238, v142
	s_add_i32 s27, s88, 0x0
	v_mfma_f32_32x32x16_bf16 v[96:111], a[216:219], a[184:187], v[96:111]
	ds_read_b64_tr_b16 v[34:35], v215 offset:0x3e00
	v_cvt_pk_bf16_f32 v141, v143, v232
	v_add_f32_e32 v143, v158, v143
	v_add_f32_e32 v158, v142, v232
	v_mfma_f32_32x32x16_bf16 v[80:95], a[248:251], a[152:155], v[80:95]
	v_cvt_pk_bf16_f32 v142, v233, v234
	v_add_f32_e32 v159, v143, v233
	v_add_f32_e32 v158, v158, v234
	v_mfma_f32_32x32x16_bf16 v[64:79], a[248:251], a[184:187], v[64:79]
	s_add_i32 s30, s88, 0x80
	v_cvt_pk_bf16_f32 v143, v239, v240
	v_add_f32_e32 v159, v159, v239
	v_add_f32_e32 v158, v158, v240
	v_mfma_f32_32x32x16_bf16 v[112:127], a[220:223], a[156:159], v[112:127]
	v_add_f32_e32 v159, v159, v148
	v_add_f32_e32 v158, v158, v149
	v_mfma_f32_32x32x16_bf16 v[96:111], a[220:223], a[188:191], v[96:111]
	s_add_i32 s31, s88, 0x800
	v_add_f32_e32 v159, v159, v150
	v_add_f32_e32 v158, v158, v151
	v_mfma_f32_32x32x16_bf16 v[80:95], a[252:255], a[156:159], v[80:95]
	v_add_f32_e32 v159, v159, v152
	v_add_f32_e32 v158, v158, v153
	v_mfma_f32_32x32x16_bf16 v[64:79], a[252:255], a[188:191], v[64:79]
	s_add_i32 s33, s88, 0x880
	v_add_f32_e32 v159, v159, v154
	v_add_f32_e32 v158, v158, v155
	v_add_f32_e32 v156, v156, v157
	s_waitcnt vmcnt(0) lgkmcnt(0)
	s_barrier
	v_mfma_f32_32x32x16_bf16 a[0:15], v[180:183], v[164:167], a[0:15]
	v_mov_b32_e32 v157, v156
	v_mfma_f32_32x32x16_bf16 a[16:31], v[180:183], v[192:195], a[16:31]
	s_nop 1
	v_permlane32_swap_b32_e32 v156, v157
	v_add_f32_e32 v156, v156, v157
	ds_read_b128 a[192:195], v217 offset:0
	v_mfma_f32_32x32x16_bf16 a[32:47], v[188:191], v[164:167], a[32:47]
	v_add_f32_e32 v219, v225, v156
	v_add_f32_e32 v156, v159, v158
	v_mov_b32_e32 v157, v156
	ds_read_b128 a[196:199], v199 offset:0
	v_mfma_f32_32x32x16_bf16 a[48:63], v[188:191], v[192:195], a[48:63]
	v_permlane32_swap_b32_e32 v156, v157
	v_add_f32_e32 v156, v156, v157
	ds_read_b128 a[200:203], v198 offset:0
	s_mov_b32 m0, s23
	v_mfma_f32_32x32x16_bf16 a[64:79], v[176:179], v[164:167], a[64:79]
	v_add_f32_e32 v218, v226, v156
	buffer_load_dwordx4 v196, s[4:7], s27 offen lds
	ds_read_b128 a[204:207], v197 offset:0
	s_mov_b32 m0, s24
	v_mfma_f32_32x32x16_bf16 a[80:95], v[176:179], v[192:195], a[80:95]
	buffer_load_dwordx4 v196, s[4:7], s30 offen lds
	ds_read_b128 a[208:211], v217 offset:128
	s_mov_b32 m0, s25
	v_mfma_f32_32x32x16_bf16 a[96:111], v[184:187], v[164:167], a[96:111]
	buffer_load_dwordx4 v196, s[4:7], s31 offen lds
	ds_read_b128 a[212:215], v199 offset:128
	s_mov_b32 m0, s26
	v_mfma_f32_32x32x16_bf16 a[112:127], v[184:187], v[192:195], a[112:127]
	buffer_load_dwordx4 v196, s[4:7], s33 offen lds
	ds_read_b128 a[216:219], v198 offset:128
	v_mfma_f32_32x32x16_bf16 a[0:15], v[172:175], v[128:131], a[0:15]
	ds_read_b128 a[220:223], v197 offset:128
	v_max3_f32 v156, v112, v113, v80
	v_max3_f32 v157, v114, v115, v81
	v_max3_f32 v156, v156, v82, v83
	v_mfma_f32_32x32x16_bf16 a[16:31], v[172:175], v[144:147], a[16:31]
	ds_read_b128 a[224:227], v217 offset:8192
	v_max3_f32 v156, v156, v116, v117
	v_max3_f32 v157, v157, v118, v119
	v_max3_f32 v156, v156, v84, v85
	v_max3_f32 v157, v157, v86, v87
	v_mfma_f32_32x32x16_bf16 a[32:47], v[168:171], v[128:131], a[32:47]
	ds_read_b128 a[228:231], v199 offset:8192
	v_max3_f32 v156, v156, v120, v121
	v_max3_f32 v157, v157, v122, v123
	v_max3_f32 v156, v156, v88, v89
	v_max3_f32 v157, v157, v90, v91
	v_mfma_f32_32x32x16_bf16 a[48:63], v[168:171], v[144:147], a[48:63]
	ds_read_b128 a[232:235], v198 offset:8192
	v_max3_f32 v156, v156, v124, v125
	v_max3_f32 v157, v157, v126, v127
	v_max3_f32 v156, v156, v92, v93
	v_max3_f32 v157, v157, v94, v95
	v_mfma_f32_32x32x16_bf16 a[64:79], v[160:163], v[128:131], a[64:79]
	ds_read_b128 a[236:239], v197 offset:8192
	v_max3_f32 v158, v96, v97, v64
	v_max3_f32 v159, v98, v99, v65
	v_max3_f32 v158, v158, v66, v67
	v_mfma_f32_32x32x16_bf16 a[80:95], v[160:163], v[144:147], a[80:95]
	ds_read_b128 a[240:243], v217 offset:8320
	v_max3_f32 v158, v158, v100, v101
	v_max3_f32 v159, v159, v102, v103
	v_max3_f32 v158, v158, v68, v69
	v_max3_f32 v159, v159, v70, v71
	v_mfma_f32_32x32x16_bf16 a[96:111], v[136:139], v[128:131], a[96:111]
	ds_read_b128 a[244:247], v199 offset:8320
	v_max3_f32 v128, v158, v104, v105
	v_max3_f32 v129, v159, v106, v107
	v_max3_f32 v128, v128, v72, v73
	v_max3_f32 v129, v129, v74, v75
	v_mfma_f32_32x32x16_bf16 a[112:127], v[136:139], v[144:147], a[112:127]
	ds_read_b128 a[248:251], v198 offset:8320
	v_max3_f32 v128, v128, v108, v109
	v_max3_f32 v129, v129, v110, v111
	v_max3_f32 v128, v128, v76, v77
	v_max3_f32 v130, v129, v78, v79
	v_mfma_f32_32x32x16_bf16 a[0:15], v[132:135], v[52:55], a[0:15]
	ds_read_b128 a[252:255], v197 offset:8320
	v_max_f32_e32 v129, v156, v157
	v_mov_b32_e32 v131, v129
	s_nop 1
	v_permlane32_swap_b32_e32 v129, v131
	v_max_f32_e32 v129, v129, v131
	v_mfma_f32_32x32x16_bf16 a[16:31], v[132:135], v[140:143], a[16:31]
	v_max_f32_e32 v128, v128, v130
	v_mov_b32_e32 v130, v128
	s_nop 1
	v_permlane32_swap_b32_e32 v128, v130
	v_max_f32_e32 v128, v128, v130
	v_max_f32_e32 v130, v129, v129
	v_max_f32_e32 v131, v128, v128
	v_max_f32_e32 v130, v130, v131
	s_mov_b32 s0, 0x41000000
	v_mfma_f32_32x32x16_bf16 a[32:47], v[60:63], v[52:55], a[32:47]
	v_cmp_lt_f32_e32 vcc, s0, v130
	s_cmp_lg_u64 vcc, 0
	s_cselect_b64 s[0:1], -1, 0
	s_cbranch_vccnz .LBB0_43
